# speedup vs baseline: 1.0032x; 1.0027x over previous
.Lattn_prio_done:
.LBB2_5:
	s_add_i32 s26, s26, 2
	v_mfma_f32_32x32x16_f16 v[96:111], v[172:175], v[124:127], v[32:47]
	v_add_u32_e32 v191, s3, v187
	ds_read_b64_tr_b16 v[176:177], v191 offset:24576
	ds_read_b64_tr_b16 v[178:179], v191 offset:25088
	v_exp_f32_e32 v56, v56
	v_exp_f32_e32 v57, v57
	v_cvt_pk_f16_f32 v140, v64, v65
	v_cvt_pk_f16_f32 v141, v66, v67
	ds_read_b64_tr_b16 v[172:173], v191 offset:28672
	ds_read_b64_tr_b16 v[174:175], v191 offset:29184
	v_mfma_f32_32x32x16_f16 v[80:95], v[168:171], v[124:127], v[32:47]
	v_exp_f32_e32 v58, v58
	v_exp_f32_e32 v59, v59
	v_pk_add_f16 v128, v140, v141
	v_cvt_pk_f16_f32 v142, v68, v69
	v_cvt_pk_f16_f32 v143, v70, v71
	ds_read_b64_tr_b16 v[64:65], v191 offset:25600
	ds_read_b64_tr_b16 v[66:67], v191 offset:26112
	v_mfma_f32_32x32x16_f16 v[96:111], v[164:167], v[120:123], v[96:111]
	v_exp_f32_e32 v60, v60
	v_exp_f32_e32 v61, v61
	v_pk_add_f16 v129, v142, v143
	v_cvt_pk_f16_f32 v136, v72, v73
	v_cvt_pk_f16_f32 v137, v74, v75
	ds_read_b64_tr_b16 v[68:69], v191 offset:29696
	ds_read_b64_tr_b16 v[70:71], v191 offset:30208
	v_mfma_f32_32x32x16_f16 v[80:95], v[160:163], v[120:123], v[80:95]
	v_exp_f32_e32 v62, v62
	v_exp_f32_e32 v63, v63
	v_pk_add_f16 v72, v136, v137
	v_pk_add_f16 v128, v128, v129
	v_cvt_pk_f16_f32 v138, v76, v77
	v_cvt_pk_f16_f32 v139, v78, v79
	s_min_u32 s2, s26, 28
	s_lshl_b32 s2, s2, 13
	s_add_u32 s2, s14, s2
	s_addc_u32 s3, s15, 0
	s_add_u32 s2, s2, 0x6000
	s_addc_u32 s3, s3, 0
	s_add_i32 s4, s31, s24
	s_mov_b32 s5, m0
	s_mov_b32 m0, s4
	s_nop 0
	global_load_lds_dwordx4 v189, s[2:3]
	s_mov_b32 m0, s5
	ds_read_b64_tr_b16 v[76:77], v191 offset:26624
	ds_read_b64_tr_b16 v[78:79], v191 offset:27136
	v_mfma_f32_32x32x16_f16 v[96:111], v[156:159], v[116:119], v[96:111]
	v_pk_add_f16 v73, v138, v139
	v_cvt_pk_f16_f32 v132, v48, v49
	v_cvt_pk_f16_f32 v133, v50, v51
	ds_read_b64_tr_b16 v[48:49], v191 offset:30720
	ds_read_b64_tr_b16 v[50:51], v191 offset:31232
	v_mfma_f32_32x32x16_f16 v[80:95], v[152:155], v[116:119], v[80:95]
	v_pk_add_f16 v129, v72, v73
	v_cvt_pk_f16_f32 v134, v52, v53
	v_cvt_pk_f16_f32 v135, v54, v55
	v_pk_add_f16 v156, v132, v133
	s_add_u32 s2, s27, 0x2000
	s_addc_u32 s3, s28, 0
	s_add_i32 s4, s29, s25
	s_mov_b32 s5, m0
	s_mov_b32 m0, s4
	s_nop 0
	global_load_lds_dwordx4 v189, s[2:3]
	s_mov_b32 m0, s5
	ds_read_b64_tr_b16 v[72:73], v191 offset:27648
	ds_read_b64_tr_b16 v[74:75], v191 offset:28160
	v_mfma_f32_32x32x16_f16 v[96:111], v[148:151], v[112:115], v[96:111]
	v_pk_add_f16 v153, v128, v129
	v_cvt_pk_f16_f32 v128, v56, v57
	v_cvt_pk_f16_f32 v129, v58, v59
	v_pk_add_f16 v152, v134, v135
	ds_read_b64_tr_b16 v[52:53], v191 offset:31744
	ds_read_b64_tr_b16 v[54:55], v191 offset:32256
	v_mfma_f32_32x32x16_f16 v[80:95], v[144:147], v[112:115], v[80:95]
	v_pk_add_f16 v56, v128, v129
	v_pk_add_f16 v57, v156, v152
	v_cvt_pk_f16_f32 v130, v60, v61
	v_cvt_pk_f16_f32 v131, v62, v63
	s_andn2_b64 vcc, exec, s[18:19]
	v_pk_add_f16 v57, v153, v57
	v_pk_add_f16 v58, v130, v131
	s_cbranch_vccnz .LBB2_7
	v_pk_add_f16 v59, v56, v58
	v_max3_f32 v61, v96, v97, v80
	v_max3_f32 v62, v98, v99, v81
	s_mov_b64 s[8:9], 0
	v_pk_add_f16 v59, v57, v59
	s_nop 0
	v_cvt_f32_f16_e32 v60, v59
	v_cvt_f32_f16_sdwa v59, v59 dst_sel:DWORD dst_unused:UNUSED_PAD src0_sel:WORD_1
	v_add_f32_e32 v59, v59, v60
	v_add_f32_e32 v188, v188, v59
	v_max3_f32 v59, v61, v82, v83
	v_max3_f32 v60, v62, v102, v103
	s_nop 0
	v_max3_f32 v59, v59, v100, v101
	v_max3_f32 v60, v60, v86, v87
	s_nop 0
	v_max3_f32 v59, v59, v84, v85
	v_max3_f32 v60, v60, v106, v107
	s_nop 0
	v_max3_f32 v59, v59, v104, v105
	v_max3_f32 v60, v60, v90, v91
	s_nop 0
	v_max3_f32 v59, v59, v88, v89
	v_max3_f32 v60, v60, v110, v111
	s_nop 0
	v_max3_f32 v59, v59, v108, v109
	v_max3_f32 v60, v60, v94, v95
	s_nop 0
	v_max3_f32 v59, v59, v92, v93
	s_nop 0
	v_max_f32 v59, v59, v60
	s_nop 0
	v_mov_b32_e32 v60, v59
	s_nop 1
	v_permlane32_swap_b32_e32 v59, v60
	v_max_f32 v59, v59, v60
	s_nop 0
	v_cmp_lt_f32_e32 vcc, s30, v59
	s_cbranch_vccnz .LBB2_19

.LBB2_11:
	s_add_i32 s33, s29, 0x2000
	s_cmpk_lg_i32 s29, 0x4000
	s_cselect_b32 s33, s33, 0
	v_mfma_f32_32x32x16_f16 v[64:79], v[56:59], v[124:127], v[32:47]
	v_add_u32_e32 v191, s31, v187
	ds_read_b64_tr_b16 v[148:149], v191 offset:24576
	ds_read_b64_tr_b16 v[150:151], v191 offset:25088
	v_exp_f32_e32 v88, v88
	v_exp_f32_e32 v89, v89
	v_cvt_pk_f16_f32 v140, v96, v97
	v_cvt_pk_f16_f32 v141, v98, v99
	ds_read_b64_tr_b16 v[144:145], v191 offset:28672
	ds_read_b64_tr_b16 v[146:147], v191 offset:29184
	s_waitcnt lgkmcnt(10)
	v_mfma_f32_32x32x16_f16 v[48:63], v[176:179], v[124:127], v[32:47]
	v_exp_f32_e32 v90, v90
	v_exp_f32_e32 v91, v91
	v_pk_add_f16 v128, v140, v141
	v_cvt_pk_f16_f32 v142, v100, v101
	v_cvt_pk_f16_f32 v143, v102, v103
	ds_read_b64_tr_b16 v[96:97], v191 offset:25600
	ds_read_b64_tr_b16 v[98:99], v191 offset:26112
	s_waitcnt lgkmcnt(11)
	v_mfma_f32_32x32x16_f16 v[64:79], v[172:175], v[120:123], v[64:79]
	v_exp_f32_e32 v92, v92
	v_exp_f32_e32 v93, v93
	v_pk_add_f16 v129, v142, v143
	v_cvt_pk_f16_f32 v136, v104, v105
	v_cvt_pk_f16_f32 v137, v106, v107
	ds_read_b64_tr_b16 v[100:101], v191 offset:29696
	ds_read_b64_tr_b16 v[102:103], v191 offset:30208
	s_waitcnt lgkmcnt(12)
	v_mfma_f32_32x32x16_f16 v[48:63], v[168:171], v[120:123], v[48:63]
	v_exp_f32_e32 v94, v94
	v_exp_f32_e32 v95, v95
	v_pk_add_f16 v128, v128, v129
	v_cvt_pk_f16_f32 v138, v108, v109
	v_cvt_pk_f16_f32 v139, v110, v111
	v_pk_add_f16 v172, v136, v137
	s_min_u32 s31, s26, 27
	s_lshl_b32 s31, s31, 13
	s_add_u32 s31, s14, s31
	s_addc_u32 s35, s15, 0
	s_add_u32 s34, s31, 0x8000
	s_addc_u32 s35, s35, 0
	s_add_i32 s31, s29, s24
	s_mov_b32 s36, m0
	s_mov_b32 m0, s31
	s_nop 0
	global_load_lds_dwordx4 v189, s[34:35]
	s_mov_b32 m0, s36
	ds_read_b64_tr_b16 v[104:105], v191 offset:26624
	ds_read_b64_tr_b16 v[106:107], v191 offset:27136
	s_waitcnt lgkmcnt(13)
	v_mfma_f32_32x32x16_f16 v[64:79], v[164:167], v[116:119], v[64:79]
	v_pk_add_f16 v108, v138, v139
	v_cvt_pk_f16_f32 v132, v80, v81
	v_cvt_pk_f16_f32 v133, v82, v83
	ds_read_b64_tr_b16 v[80:81], v191 offset:30720
	ds_read_b64_tr_b16 v[82:83], v191 offset:31232
	s_waitcnt lgkmcnt(14)
	v_mfma_f32_32x32x16_f16 v[48:63], v[160:163], v[116:119], v[48:63]
	v_pk_add_f16 v129, v172, v108
	v_cvt_pk_f16_f32 v134, v84, v85
	v_cvt_pk_f16_f32 v135, v86, v87
	v_pk_add_f16 v164, v132, v133
	s_add_u32 s34, s27, 0x4000
	s_addc_u32 s35, s28, 0
	s_add_i32 s31, s33, s25
	s_mov_b32 s36, m0
	s_mov_b32 m0, s31
	s_nop 0
	global_load_lds_dwordx4 v189, s[34:35]
	s_mov_b32 m0, s36
	ds_read_b64_tr_b16 v[108:109], v191 offset:27648
	ds_read_b64_tr_b16 v[110:111], v191 offset:28160
	s_waitcnt lgkmcnt(14)
	v_mfma_f32_32x32x16_f16 v[64:79], v[156:159], v[112:115], v[64:79]
	v_pk_add_f16 v161, v128, v129
	v_cvt_pk_f16_f32 v128, v88, v89
	v_cvt_pk_f16_f32 v129, v90, v91
	v_pk_add_f16 v160, v134, v135
	ds_read_b64_tr_b16 v[84:85], v191 offset:31744
	ds_read_b64_tr_b16 v[86:87], v191 offset:32256
	v_mfma_f32_32x32x16_f16 v[48:63], v[152:155], v[112:115], v[48:63]
	v_pk_add_f16 v88, v128, v129
	v_pk_add_f16 v89, v164, v160
	v_cvt_pk_f16_f32 v130, v92, v93
	v_cvt_pk_f16_f32 v131, v94, v95
	s_and_b64 vcc, exec, s[16:17]
	v_pk_add_f16 v89, v161, v89
	v_pk_add_f16 v90, v130, v131
	s_cbranch_vccnz .LBB2_13
	v_pk_add_f16 v91, v88, v90
	v_max3_f32 v93, v64, v65, v48
	v_max3_f32 v94, v66, v67, v49
	s_mov_b64 s[8:9], 0
	v_pk_add_f16 v91, v89, v91
	s_nop 0
	v_cvt_f32_f16_e32 v92, v91
	v_cvt_f32_f16_sdwa v91, v91 dst_sel:DWORD dst_unused:UNUSED_PAD src0_sel:WORD_1
	v_add_f32_e32 v91, v91, v92
	v_add_f32_e32 v188, v188, v91
	v_max3_f32 v91, v93, v50, v51
	v_max3_f32 v92, v94, v70, v71
	s_nop 0
	v_max3_f32 v91, v91, v68, v69
	v_max3_f32 v92, v92, v54, v55
	s_nop 0
	v_max3_f32 v91, v91, v52, v53
	v_max3_f32 v92, v92, v74, v75
	s_nop 0
	v_max3_f32 v91, v91, v72, v73
	v_max3_f32 v92, v92, v58, v59
	s_nop 0
	v_max3_f32 v91, v91, v56, v57
	v_max3_f32 v92, v92, v78, v79
	s_nop 0
	v_max3_f32 v91, v91, v76, v77
	v_max3_f32 v92, v92, v62, v63
	s_nop 0
	v_max3_f32 v91, v91, v60, v61
	s_nop 0
	v_max_f32 v91, v91, v92
	s_nop 0
	v_mov_b32_e32 v92, v91
	s_nop 1
	v_permlane32_swap_b32_e32 v91, v92
	v_max_f32 v91, v91, v92
	s_nop 0
	v_cmp_lt_f32_e32 vcc, s30, v91
	s_cbranch_vccnz .LBB2_22
